# NSA tile loop: first PV k-step (4 reads + 4 MFMA) moved to the end of the softmax segment; other three stay with DMA/QK
# speedup vs baseline: 1.0013x; 1.0013x over previous
; #define LAS __attribute__((address_space(3)))
; __device__ __forceinline__ bf16x8 nsa_pack8(const f32x16& p, int s) { u32x4 w; w.x = pg8::cvt_pk_bf16(p[8 * s + 0], p[8 * s + 1]); w.y = pg8::cvt_pk_bf16(p[8 * s + 2], p[8 * s + 3]); w.z = pg8::cvt_pk_bf16(p[8 * s + 4], p[8 * s + 5]); w.w = pg8::cvt_pk_bf16(p[8 * s + 6], p[8 * s + 7]); return __builtin_bit_cast(bf16x8, w); }
; __device__ __forceinline__ void nsa_pv_rd4(const LAS unsigned char* vA, int sv, int step, bf16x8 (&af)[4]) {
; #pragma unroll
;     for (int dt = 0; dt < 4; ++dt) af[dt] = *(const LAS bf16x8*)(vA + dt * 4096 + (((2 * step) * 16) ^ sv));
; }
; __device__ __forceinline__ void nsa_pv_mm4(const bf16x8 (&af)[4], const bf16x8& pfk, f32x16 (&o)[4]) {
; #pragma unroll
;     for (int dt = 0; dt < 4; ++dt) o[dt] = __builtin_amdgcn_mfma_f32_32x32x16_bf16(af[dt], pfk, o[dt], 0, 0, 0);
; }
; __device__ __forceinline__ void nsa_pv_sw(const LAS unsigned char* vbuf, const bf16x8 (&pf)[2][2], f32x16 (&o)[4], int r, int h) {
;     const int sv = (((r >> 1) & 7) ^ h) * 16; const LAS unsigned char* vA = vbuf + r * 128;
; #pragma unroll
;     for (int step = 0; step < 4; ++step) { bf16x8 fa[4];
;         nsa_pv_rd4(vA, sv, step, fa); __builtin_amdgcn_sched_barrier(0);
;         nsa_pv_mm4(fa, pf[step >> 1][step & 1], o); __builtin_amdgcn_sched_barrier(0); }
; __device__ __forceinline__ void nsa_unit(const Args& a, LAS unsigned char* lds, int b, int kvh, int qb) {
;     ...
;             const float nmc = lane_on ? -mrun * SM_C : NINF;
;             float ls = 0.f;
; #pragma unroll
;             for (int i = 0; i < 16; ++i) { p0[i] = __builtin_amdgcn_exp2f(fmaf(p0[i], SM_C, nmc)); p1[i] = __builtin_amdgcn_exp2f(fmaf(p1[i], SM_C, nmc)); ls += p0[i] + p1[i]; }
;             lrun = lrun * alpha + ls;
;             pf[0][0] = nsa_pack8(p0, 0); pf[0][1] = nsa_pack8(p0, 1); pf[1][0] = nsa_pack8(p1, 0); pf[1][1] = nsa_pack8(p1, 1);
.LBB0_911:
	v_mul_f32_e32 v34, 0xbe0293ee, v208
	v_cndmask_b32_e64 v190, v244, v34, s[2:3]
	v_fmamk_f32 v34, v78, 0x3e0293ee, v190
	v_exp_f32_e32 v78, v34
	v_fmamk_f32 v34, v62, 0x3e0293ee, v190
	v_exp_f32_e32 v62, v34
	v_fmamk_f32 v34, v79, 0x3e0293ee, v190
	v_fmamk_f32 v36, v80, 0x3e0293ee, v190
	v_exp_f32_e32 v79, v34
	v_fmamk_f32 v34, v63, 0x3e0293ee, v190
	v_exp_f32_e32 v80, v36
	v_fmamk_f32 v36, v64, 0x3e0293ee, v190
	v_exp_f32_e32 v63, v34
	v_exp_f32_e32 v64, v36
	v_fmamk_f32 v36, v81, 0x3e0293ee, v190
	v_exp_f32_e32 v81, v36
	v_fmamk_f32 v36, v65, 0x3e0293ee, v190
	v_exp_f32_e32 v65, v36
	v_add_f32_e32 v34, v78, v62
	v_add_f32_e32 v34, 0, v34
	v_add_f32_e32 v35, v79, v63
	v_add_f32_e32 v34, v35, v34
	v_add_f32_e32 v35, v80, v64
	v_add_f32_e32 v34, v35, v34
	v_add_f32_e32 v35, v81, v65
	v_add_f32_e32 v50, v35, v34
	v_fmamk_f32 v34, v82, 0x3e0293ee, v190
	v_exp_f32_e32 v35, v34
	v_fmamk_f32 v34, v66, 0x3e0293ee, v190
	v_exp_f32_e32 v37, v34
	v_fmamk_f32 v34, v83, 0x3e0293ee, v190
	v_fmamk_f32 v36, v67, 0x3e0293ee, v190
	v_fmamk_f32 v38, v84, 0x3e0293ee, v190
	v_exp_f32_e32 v34, v34
	v_exp_f32_e32 v36, v36
	v_exp_f32_e32 v39, v38
	v_fmamk_f32 v38, v68, 0x3e0293ee, v190
	v_exp_f32_e32 v41, v38
	v_fmamk_f32 v38, v85, 0x3e0293ee, v190
	v_fmamk_f32 v40, v69, 0x3e0293ee, v190
	v_exp_f32_e32 v38, v38
	v_exp_f32_e32 v40, v40
	v_pk_add_f32 v[48:49], v[34:35], v[36:37]
	v_fmamk_f32 v52, v88, 0x3e0293ee, v190
	v_add_f32_e32 v49, v49, v50
	v_add_f32_e32 v50, v48, v49
	v_pk_add_f32 v[48:49], v[38:39], v[40:41]
	v_exp_f32_e32 v53, v52
	v_add_f32_e32 v49, v49, v50
	v_add_f32_e32 v58, v48, v49
	v_fmamk_f32 v48, v86, 0x3e0293ee, v190
	v_exp_f32_e32 v49, v48
	v_fmamk_f32 v48, v70, 0x3e0293ee, v190
	v_exp_f32_e32 v51, v48
	v_fmamk_f32 v48, v87, 0x3e0293ee, v190
	v_fmamk_f32 v50, v71, 0x3e0293ee, v190
	v_exp_f32_e32 v48, v48
	v_exp_f32_e32 v50, v50
	v_fmamk_f32 v52, v72, 0x3e0293ee, v190
	v_exp_f32_e32 v55, v52
	v_fmamk_f32 v52, v89, 0x3e0293ee, v190
	v_fmamk_f32 v54, v73, 0x3e0293ee, v190
	v_exp_f32_e32 v52, v52
	v_exp_f32_e32 v54, v54
	v_pk_add_f32 v[56:57], v[48:49], v[50:51]
	v_fmamk_f32 v60, v92, 0x3e0293ee, v190
	v_add_f32_e32 v57, v57, v58
	v_add_f32_e32 v58, v56, v57
	v_pk_add_f32 v[56:57], v[52:53], v[54:55]
	v_exp_f32_e32 v61, v60
	v_add_f32_e32 v57, v57, v58
	v_add_f32_e32 v68, v56, v57
	v_fmamk_f32 v56, v90, 0x3e0293ee, v190
	v_exp_f32_e32 v57, v56
	v_fmamk_f32 v56, v74, 0x3e0293ee, v190
	v_exp_f32_e32 v59, v56
	v_fmamk_f32 v56, v91, 0x3e0293ee, v190
	v_fmamk_f32 v58, v75, 0x3e0293ee, v190
	v_exp_f32_e32 v56, v56
	v_exp_f32_e32 v58, v58
	v_fmamk_f32 v60, v76, 0x3e0293ee, v190
	v_exp_f32_e32 v211, v60
	v_fmamk_f32 v60, v93, 0x3e0293ee, v190
	v_fmac_f32_e32 v190, 0x3e0293ee, v77
	v_exp_f32_e32 v60, v60
	v_exp_f32_e32 v210, v190
	v_pk_add_f32 v[66:67], v[56:57], v[58:59]
	v_add_f32_e32 v67, v67, v68
	v_add_f32_e32 v66, v66, v67
	v_pk_add_f32 v[190:191], v[60:61], v[210:211]
	v_add_f32_e32 v191, v191, v66
	v_add_f32_e32 v212, v190, v191
	v_fmac_f32_e32 v212, v209, v46
	v_mov_b32_e32 v209, v212
	v_cvt_pk_bf16_f32 v190, v78, v79
	v_cvt_pk_bf16_f32 v191, v80, v81
	v_cvt_pk_bf16_f32 v192, v35, v34
	v_cvt_pk_bf16_f32 v193, v39, v38
	v_cvt_pk_bf16_f32 v194, v49, v48
	v_cvt_pk_bf16_f32 v195, v53, v52
	v_cvt_pk_bf16_f32 v196, v57, v56
	v_cvt_pk_bf16_f32 v197, v61, v60
	v_cvt_pk_bf16_f32 v198, v62, v63
	v_cvt_pk_bf16_f32 v199, v64, v65
	v_cvt_pk_bf16_f32 v200, v37, v36
	v_cvt_pk_bf16_f32 v201, v41, v40
	v_cvt_pk_bf16_f32 v202, v51, v50
	v_cvt_pk_bf16_f32 v203, v55, v54
	v_cvt_pk_bf16_f32 v204, v59, v58
	v_cvt_pk_bf16_f32 v205, v211, v210
	v_mov_b32_e32 v211, v233
	v_mov_b32_e32 v210, v232
	s_and_b32 s33, s75, 0xc000
	v_lshrrev_b32_e32 v34, 1, v210
	s_add_i32 s33, s33, 0
	v_bitop3_b32 v34, v34, v211, 7 bitop3:0x6c
	v_lshlrev_b32_e32 v46, 4, v34
	v_lshl_add_u32 v56, v210, 7, s33
	v_add_u32_e32 v212, v56, v46
	ds_read_b128 v[34:37], v212 offset:49152
	ds_read_b128 v[38:41], v212 offset:53248
	ds_read_b128 v[48:51], v212 offset:57344
	ds_read_b128 v[52:55], v212 offset:61440
	s_waitcnt lgkmcnt(3)
	v_mfma_f32_32x32x16_bf16 v[142:157], v[34:37], v[190:193], v[142:157]
	s_waitcnt lgkmcnt(2)
	v_mfma_f32_32x32x16_bf16 v[126:141], v[38:41], v[190:193], v[126:141]
	s_waitcnt lgkmcnt(1)
	v_mfma_f32_32x32x16_bf16 v[110:125], v[48:51], v[190:193], v[110:125]
	s_waitcnt lgkmcnt(0)
	v_mfma_f32_32x32x16_bf16 v[94:109], v[52:55], v[190:193], v[94:109]

; #define GAS __attribute__((address_space(1)))
; #define LAS __attribute__((address_space(3)))
; __device__ __forceinline__ unsigned cvt_pk_bf16(float lo, float hi) { unsigned r; asm volatile("v_cvt_pk_bf16_f32 %0, %1, %2" : "=v"(r) : "v"(lo), "v"(hi)); return r; }
; __device__ __forceinline__ void nsa_pv_rd4(const LAS unsigned char* vA, int sv, int step, bf16x8 (&af)[4]) {
; #pragma unroll
;     for (int dt = 0; dt < 4; ++dt) af[dt] = *(const LAS bf16x8*)(vA + dt * 4096 + (((2 * step) * 16) ^ sv));
; }
; __device__ __forceinline__ void nsa_pv_mm4(const bf16x8 (&af)[4], const bf16x8& pfk, f32x16 (&o)[4]) {
; #pragma unroll
;     for (int dt = 0; dt < 4; ++dt) o[dt] = __builtin_amdgcn_mfma_f32_32x32x16_bf16(af[dt], pfk, o[dt], 0, 0, 0);
; }
; __device__ __forceinline__ void nsa_pv_sw(const LAS unsigned char* vbuf, const bf16x8 (&pf)[2][2], f32x16 (&o)[4], int r, int h) {
;     const int sv = (((r >> 1) & 7) ^ h) * 16; const LAS unsigned char* vA = vbuf + r * 128;
; #pragma unroll
;     for (int step = 0; step < 4; ++step) { bf16x8 fa[4];
;         nsa_pv_rd4(vA, sv, step, fa); __builtin_amdgcn_sched_barrier(0);
;         nsa_pv_mm4(fa, pf[step >> 1][step & 1], o); __builtin_amdgcn_sched_barrier(0); }
; __device__ __forceinline__ void nsa_unit(const Args& a, LAS unsigned char* lds, int b, int kvh, int qb) {
;     ...
;         int ro = r, ho = h; asm volatile("" : "+v"(ro), "+v"(ho));
;         if (it > 0) { const int ti = it - 1;
;             nsa_pv_sw(lds + VOFF + (ti & 3) * NTB, pf, o, ro, ho);
;             if (ti == nS - 1 || ti == nTot - 1) {
;                 const float lt = lrun + __shfl_xor(lrun, 32); const float f = ((ti == nS - 1) ? g1 : g2) / lt;
; #pragma unroll
;                 for (int dt = 0; dt < 4; ++dt) {
; #pragma unroll
;                     for (int aa = 0; aa < 4; ++aa) { const u32x2 pv = *(const GAS u32x2*)(mp + (32 * dt + 8 * aa) * 2); u32x2 wv;
;                         wv.x = pg8::cvt_pk_bf16(bflo(pv.x) + o[dt][4 * aa] * f, bfhi(pv.x) + o[dt][4 * aa + 1] * f); wv.y = pg8::cvt_pk_bf16(bflo(pv.y) + o[dt][4 * aa + 2] * f, bfhi(pv.y) + o[dt][4 * aa + 3] * f);
;                         *(GAS u32x2*)(mp + (32 * dt + 8 * aa) * 2) = wv; }
.LBB0_914:
	v_mov_b32_e32 v211, v233
	v_mov_b32_e32 v210, v232
	s_andn2_b64 vcc, exec, s[0:1]
	s_cbranch_vccnz .LBB0_917
	s_and_b32 s0, s75, 0xc000
	v_lshrrev_b32_e32 v34, 1, v210
	s_add_i32 s0, s0, 0
	v_bitop3_b32 v34, v34, v211, 7 bitop3:0x6c
	v_lshlrev_b32_e32 v46, 4, v34
	v_lshl_add_u32 v56, v210, 7, s0
	v_xad_u32 v213, v46, 32, v56
	v_xad_u32 v214, v46, 64, v56
	v_xad_u32 v215, v46, s68, v56
	ds_read_b128 v[62:65], v213 offset:49152
	ds_read_b128 v[66:69], v213 offset:53248
	ds_read_b128 v[70:73], v213 offset:57344
	ds_read_b128 v[74:77], v213 offset:61440
	ds_read_b128 v[78:81], v214 offset:49152
	ds_read_b128 v[82:85], v214 offset:53248
	ds_read_b128 v[86:89], v214 offset:57344
	ds_read_b128 v[90:93], v214 offset:61440
	ds_read_b128 v[34:37], v215 offset:49152
	ds_read_b128 v[38:41], v215 offset:53248
	ds_read_b128 v[48:51], v215 offset:57344
	ds_read_b128 v[52:55], v215 offset:61440
	s_waitcnt lgkmcnt(11)
	v_mfma_f32_32x32x16_bf16 v[142:157], v[62:65], v[194:197], v[142:157]
	s_waitcnt lgkmcnt(10)
	v_mfma_f32_32x32x16_bf16 v[126:141], v[66:69], v[194:197], v[126:141]
	s_waitcnt lgkmcnt(9)
	v_mfma_f32_32x32x16_bf16 v[110:125], v[70:73], v[194:197], v[110:125]
	s_waitcnt lgkmcnt(8)
	v_mfma_f32_32x32x16_bf16 v[94:109], v[74:77], v[194:197], v[94:109]
	s_waitcnt lgkmcnt(7)
	v_mfma_f32_32x32x16_bf16 v[142:157], v[78:81], v[198:201], v[142:157]
	s_waitcnt lgkmcnt(6)
	v_mfma_f32_32x32x16_bf16 v[126:141], v[82:85], v[198:201], v[126:141]
	s_waitcnt lgkmcnt(5)
	v_mfma_f32_32x32x16_bf16 v[110:125], v[86:89], v[198:201], v[110:125]
	s_waitcnt lgkmcnt(4)
	v_mfma_f32_32x32x16_bf16 v[94:109], v[90:93], v[198:201], v[94:109]
	s_waitcnt lgkmcnt(3)
	v_mfma_f32_32x32x16_bf16 v[142:157], v[34:37], v[202:205], v[142:157]
	s_waitcnt lgkmcnt(2)
	v_mfma_f32_32x32x16_bf16 v[126:141], v[38:41], v[202:205], v[126:141]
	s_waitcnt lgkmcnt(1)
	v_mfma_f32_32x32x16_bf16 v[110:125], v[48:51], v[202:205], v[110:125]
	s_waitcnt lgkmcnt(0)
	v_mfma_f32_32x32x16_bf16 v[94:109], v[52:55], v[202:205], v[94:109]
	s_cmp_eq_u32 s14, s74
	s_cselect_b64 s[12:13], -1, 0
	s_cmp_eq_u32 s24, s74
	s_cselect_b64 s[0:1], -1, 0
	s_or_b64 s[0:1], s[12:13], s[0:1]
	s_andn2_b64 vcc, exec, s[0:1]
	s_cbranch_vccnz .LBB0_917
	ds_bpermute_b32 v229, v252, v209
	v_cndmask_b32_e64 v208, v251, v250, s[12:13]
	v_mov_b32_e32 v60, v47
	v_mov_b32_e32 v61, v47
	v_mov_b32_e32 v48, v47
	s_waitcnt lgkmcnt(0)
	v_pk_add_f32 v[34:35], v[208:209], v[228:229]
	v_mov_b32_e32 v49, v47
	v_div_scale_f32 v36, s[0:1], v34, v34, 1.0
	v_rcp_f32_e32 v37, v36
	v_mov_b32_e32 v50, v47
	v_mov_b32_e32 v51, v47
	v_mov_b32_e32 v52, v47
	v_fma_f32 v38, -v36, v37, 1.0
	v_fmac_f32_e32 v37, v38, v37
	v_div_scale_f32 v38, vcc, 1.0, v34, 1.0
	v_mul_f32_e32 v39, v38, v37
	v_fma_f32 v40, -v36, v39, v38
	v_fmac_f32_e32 v39, v40, v37
	v_fma_f32 v36, -v36, v39, v38
	v_div_fmas_f32 v36, v36, v37, v39
	v_div_fixup_f32 v34, v36, v34, 1.0
	v_div_scale_f32 v36, s[0:1], v35, v35, v34
	v_rcp_f32_e32 v37, v36
	v_mov_b32_e32 v53, v47
	v_mov_b32_e32 v54, v47
	v_mov_b32_e32 v55, v47
	v_fma_f32 v38, -v36, v37, 1.0
	v_fmac_f32_e32 v37, v38, v37
	v_div_scale_f32 v38, vcc, v34, v35, v34
	v_mul_f32_e32 v39, v38, v37
	v_fma_f32 v40, -v36, v39, v38
	v_fmac_f32_e32 v39, v40, v37
	v_fma_f32 v36, -v36, v39, v38
	v_div_fmas_f32 v36, v36, v37, v39
	v_div_fixup_f32 v46, v36, v35, v34
	v_mov_b32_e32 v56, v47
	v_mov_b32_e32 v57, v47
	v_mov_b32_e32 v58, v47
	v_mov_b32_e32 v59, v47
	v_mov_b32_e32 v208, 0xf149f2ca
	v_mov_b32_e32 v209, 0
	global_load_dwordx2 v[62:63], v[206:207], off
	global_load_dwordx2 v[64:65], v[206:207], off offset:16
	global_load_dwordx2 v[66:67], v[206:207], off offset:32
	global_load_dwordx2 v[68:69], v[206:207], off offset:48
	global_load_dwordx2 v[70:71], v[206:207], off offset:64
	global_load_dwordx2 v[72:73], v[206:207], off offset:80
	global_load_dwordx2 v[74:75], v[206:207], off offset:96
	global_load_dwordx2 v[76:77], v[206:207], off offset:112
	global_load_dwordx2 v[78:79], v[206:207], off offset:128
	global_load_dwordx2 v[80:81], v[206:207], off offset:144
	global_load_dwordx2 v[82:83], v[206:207], off offset:160
	global_load_dwordx2 v[84:85], v[206:207], off offset:176
	global_load_dwordx2 v[86:87], v[206:207], off offset:192
	global_load_dwordx2 v[88:89], v[206:207], off offset:208
	global_load_dwordx2 v[90:91], v[206:207], off offset:224
	global_load_dwordx2 v[92:93], v[206:207], off offset:240
	s_waitcnt vmcnt(15)
	v_lshlrev_b32_e32 v36, 16, v62
	v_and_b32_e32 v34, 0xffff0000, v62
	v_fmac_f32_e32 v36, v142, v46
	v_fmac_f32_e32 v34, v143, v46
	v_cvt_pk_bf16_f32 v34, v36, v34
	v_lshlrev_b32_e32 v36, 16, v63
	v_and_b32_e32 v35, 0xffff0000, v63
	v_fmac_f32_e32 v35, v145, v46
	v_fmac_f32_e32 v36, v144, v46
	v_cvt_pk_bf16_f32 v35, v36, v35
	global_store_dwordx2 v[206:207], v[34:35], off
	s_waitcnt vmcnt(15)
	v_lshlrev_b32_e32 v36, 16, v64
	v_and_b32_e32 v34, 0xffff0000, v64
	v_fmac_f32_e32 v36, v146, v46
	v_fmac_f32_e32 v34, v147, v46
	v_cvt_pk_bf16_f32 v34, v36, v34
	v_lshlrev_b32_e32 v36, 16, v65
	v_and_b32_e32 v35, 0xffff0000, v65
	v_fmac_f32_e32 v35, v149, v46
	v_fmac_f32_e32 v36, v148, v46
	v_cvt_pk_bf16_f32 v35, v36, v35
	global_store_dwordx2 v[206:207], v[34:35], off offset:16
	s_waitcnt vmcnt(15)
	v_lshlrev_b32_e32 v36, 16, v66
	v_and_b32_e32 v34, 0xffff0000, v66
	v_fmac_f32_e32 v36, v150, v46
	v_fmac_f32_e32 v34, v151, v46
	v_cvt_pk_bf16_f32 v34, v36, v34
	v_lshlrev_b32_e32 v36, 16, v67
	v_and_b32_e32 v35, 0xffff0000, v67
	v_fmac_f32_e32 v35, v153, v46
	v_fmac_f32_e32 v36, v152, v46
	v_cvt_pk_bf16_f32 v35, v36, v35
	global_store_dwordx2 v[206:207], v[34:35], off offset:32
	s_waitcnt vmcnt(15)
; #define GAS __attribute__((address_space(1)))
; __device__ __forceinline__ unsigned cvt_pk_bf16(float lo, float hi) { unsigned r; asm volatile("v_cvt_pk_bf16_f32 %0, %1, %2" : "=v"(r) : "v"(lo), "v"(hi)); return r; }
; __device__ __forceinline__ void nsa_unit(const Args& a, LAS unsigned char* lds, int b, int kvh, int qb) {
;     ...
;                 const float lt = lrun + __shfl_xor(lrun, 32); const float f = ((ti == nS - 1) ? g1 : g2) / lt;
; #pragma unroll
;                 for (int dt = 0; dt < 4; ++dt) {
; #pragma unroll
;                     for (int aa = 0; aa < 4; ++aa) { const u32x2 pv = *(const GAS u32x2*)(mp + (32 * dt + 8 * aa) * 2); u32x2 wv;
;                         wv.x = pg8::cvt_pk_bf16(bflo(pv.x) + o[dt][4 * aa] * f, bfhi(pv.x) + o[dt][4 * aa + 1] * f); wv.y = pg8::cvt_pk_bf16(bflo(pv.y) + o[dt][4 * aa + 2] * f, bfhi(pv.y) + o[dt][4 * aa + 3] * f);
;                         *(GAS u32x2*)(mp + (32 * dt + 8 * aa) * 2) = wv; }
; #pragma unroll
;                     for (int i = 0; i < 16; ++i) o[dt][i] = 0.f; }
;                 mrun = -1e30f; lrun = 0.f;
;                 asm volatile("s_waitcnt vmcnt(0)" ::: "memory");
	v_lshlrev_b32_e32 v36, 16, v68
	v_and_b32_e32 v34, 0xffff0000, v68
	v_fmac_f32_e32 v36, v154, v46
	v_fmac_f32_e32 v34, v155, v46
	v_cvt_pk_bf16_f32 v34, v36, v34
	v_lshlrev_b32_e32 v36, 16, v69
	v_and_b32_e32 v35, 0xffff0000, v69
	v_fmac_f32_e32 v35, v157, v46
	v_fmac_f32_e32 v36, v156, v46
	v_cvt_pk_bf16_f32 v35, v36, v35
	global_store_dwordx2 v[206:207], v[34:35], off offset:48
	s_waitcnt vmcnt(15)
	v_lshlrev_b32_e32 v36, 16, v70
	v_and_b32_e32 v34, 0xffff0000, v70
	v_fmac_f32_e32 v36, v126, v46
	v_fmac_f32_e32 v34, v127, v46
	v_cvt_pk_bf16_f32 v34, v36, v34
	v_lshlrev_b32_e32 v36, 16, v71
	v_and_b32_e32 v35, 0xffff0000, v71
	v_fmac_f32_e32 v35, v129, v46
	v_fmac_f32_e32 v36, v128, v46
	v_cvt_pk_bf16_f32 v35, v36, v35
	global_store_dwordx2 v[206:207], v[34:35], off offset:64
	s_waitcnt vmcnt(15)
	v_lshlrev_b32_e32 v36, 16, v72
	v_and_b32_e32 v34, 0xffff0000, v72
	v_fmac_f32_e32 v36, v130, v46
	v_fmac_f32_e32 v34, v131, v46
	v_cvt_pk_bf16_f32 v34, v36, v34
	v_lshlrev_b32_e32 v36, 16, v73
	v_and_b32_e32 v35, 0xffff0000, v73
	v_fmac_f32_e32 v35, v133, v46
	v_fmac_f32_e32 v36, v132, v46
	v_cvt_pk_bf16_f32 v35, v36, v35
	global_store_dwordx2 v[206:207], v[34:35], off offset:80
	s_waitcnt vmcnt(15)
	v_lshlrev_b32_e32 v36, 16, v74
	v_and_b32_e32 v34, 0xffff0000, v74
	v_fmac_f32_e32 v36, v134, v46
	v_fmac_f32_e32 v34, v135, v46
	v_cvt_pk_bf16_f32 v34, v36, v34
	v_lshlrev_b32_e32 v36, 16, v75
	v_and_b32_e32 v35, 0xffff0000, v75
	v_fmac_f32_e32 v35, v137, v46
	v_fmac_f32_e32 v36, v136, v46
	v_cvt_pk_bf16_f32 v35, v36, v35
	global_store_dwordx2 v[206:207], v[34:35], off offset:96
	s_waitcnt vmcnt(15)
	v_lshlrev_b32_e32 v36, 16, v76
	v_and_b32_e32 v34, 0xffff0000, v76
	v_fmac_f32_e32 v36, v138, v46
	v_fmac_f32_e32 v34, v139, v46
	v_cvt_pk_bf16_f32 v34, v36, v34
	v_lshlrev_b32_e32 v36, 16, v77
	v_and_b32_e32 v35, 0xffff0000, v77
	v_fmac_f32_e32 v35, v141, v46
	v_fmac_f32_e32 v36, v140, v46
	v_cvt_pk_bf16_f32 v35, v36, v35
	global_store_dwordx2 v[206:207], v[34:35], off offset:112
	s_waitcnt vmcnt(15)
	v_lshlrev_b32_e32 v36, 16, v78
	v_and_b32_e32 v34, 0xffff0000, v78
	v_fmac_f32_e32 v36, v110, v46
	v_fmac_f32_e32 v34, v111, v46
	v_cvt_pk_bf16_f32 v34, v36, v34
	v_lshlrev_b32_e32 v36, 16, v79
	v_and_b32_e32 v35, 0xffff0000, v79
	v_fmac_f32_e32 v35, v113, v46
	v_fmac_f32_e32 v36, v112, v46
	v_cvt_pk_bf16_f32 v35, v36, v35
	global_store_dwordx2 v[206:207], v[34:35], off offset:128
	s_waitcnt vmcnt(15)
	v_lshlrev_b32_e32 v36, 16, v80
	v_and_b32_e32 v34, 0xffff0000, v80
	v_fmac_f32_e32 v36, v114, v46
	v_fmac_f32_e32 v34, v115, v46
	v_cvt_pk_bf16_f32 v34, v36, v34
	v_lshlrev_b32_e32 v36, 16, v81
	v_and_b32_e32 v35, 0xffff0000, v81
	v_fmac_f32_e32 v35, v117, v46
	v_fmac_f32_e32 v36, v116, v46
	v_cvt_pk_bf16_f32 v35, v36, v35
	global_store_dwordx2 v[206:207], v[34:35], off offset:144
	s_waitcnt vmcnt(15)
	v_lshlrev_b32_e32 v36, 16, v82
	v_and_b32_e32 v34, 0xffff0000, v82
	v_fmac_f32_e32 v36, v118, v46
	v_fmac_f32_e32 v34, v119, v46
	v_cvt_pk_bf16_f32 v34, v36, v34
	v_lshlrev_b32_e32 v36, 16, v83
	v_and_b32_e32 v35, 0xffff0000, v83
	v_fmac_f32_e32 v35, v121, v46
	v_fmac_f32_e32 v36, v120, v46
	v_cvt_pk_bf16_f32 v35, v36, v35
	global_store_dwordx2 v[206:207], v[34:35], off offset:160
	s_waitcnt vmcnt(15)
	v_lshlrev_b32_e32 v36, 16, v84
	v_and_b32_e32 v34, 0xffff0000, v84
	v_fmac_f32_e32 v36, v122, v46
	v_fmac_f32_e32 v34, v123, v46
	v_cvt_pk_bf16_f32 v34, v36, v34
	v_lshlrev_b32_e32 v36, 16, v85
	v_and_b32_e32 v35, 0xffff0000, v85
	v_fmac_f32_e32 v35, v125, v46
	v_fmac_f32_e32 v36, v124, v46
	v_cvt_pk_bf16_f32 v35, v36, v35
	global_store_dwordx2 v[206:207], v[34:35], off offset:176
	s_waitcnt vmcnt(15)
	v_lshlrev_b32_e32 v36, 16, v86
	v_and_b32_e32 v34, 0xffff0000, v86
	v_fmac_f32_e32 v36, v94, v46
	v_fmac_f32_e32 v34, v95, v46
	v_cvt_pk_bf16_f32 v34, v36, v34
	v_lshlrev_b32_e32 v36, 16, v87
	v_and_b32_e32 v35, 0xffff0000, v87
	v_fmac_f32_e32 v35, v97, v46
	v_fmac_f32_e32 v36, v96, v46
	v_cvt_pk_bf16_f32 v35, v36, v35
	global_store_dwordx2 v[206:207], v[34:35], off offset:192
	s_waitcnt vmcnt(15)
	v_lshlrev_b32_e32 v36, 16, v88
	v_and_b32_e32 v34, 0xffff0000, v88
	v_fmac_f32_e32 v36, v98, v46
	v_fmac_f32_e32 v34, v99, v46
	v_cvt_pk_bf16_f32 v34, v36, v34
	v_lshlrev_b32_e32 v36, 16, v89
	v_and_b32_e32 v35, 0xffff0000, v89
	v_fmac_f32_e32 v35, v101, v46
	v_fmac_f32_e32 v36, v100, v46
	v_cvt_pk_bf16_f32 v35, v36, v35
	global_store_dwordx2 v[206:207], v[34:35], off offset:208
	s_waitcnt vmcnt(15)
	v_lshlrev_b32_e32 v36, 16, v90
	v_and_b32_e32 v34, 0xffff0000, v90
	v_fmac_f32_e32 v36, v102, v46
	v_fmac_f32_e32 v34, v103, v46
	v_cvt_pk_bf16_f32 v34, v36, v34
	v_lshlrev_b32_e32 v36, 16, v91
	v_and_b32_e32 v35, 0xffff0000, v91
	v_fmac_f32_e32 v35, v105, v46
	v_fmac_f32_e32 v36, v104, v46
	v_cvt_pk_bf16_f32 v35, v36, v35
	global_store_dwordx2 v[206:207], v[34:35], off offset:224
	s_waitcnt vmcnt(15)
	v_lshlrev_b32_e32 v36, 16, v92
	v_and_b32_e32 v34, 0xffff0000, v92
	v_fmac_f32_e32 v36, v106, v46
	v_fmac_f32_e32 v34, v107, v46
	v_cvt_pk_bf16_f32 v34, v36, v34
	v_lshlrev_b32_e32 v36, 16, v93
	v_and_b32_e32 v35, 0xffff0000, v93
	v_fmac_f32_e32 v35, v109, v46
	v_fmac_f32_e32 v36, v108, v46
	v_cvt_pk_bf16_f32 v35, v36, v35
	global_store_dwordx2 v[206:207], v[34:35], off offset:240
	s_waitcnt vmcnt(0)
	v_mov_b32_e32 v46, v47
	v_mov_b64_e32 v[156:157], v[60:61]
	v_mov_b64_e32 v[140:141], v[60:61]
	v_mov_b64_e32 v[124:125], v[60:61]
	v_mov_b64_e32 v[108:109], v[60:61]
	v_mov_b64_e32 v[154:155], v[58:59]
	v_mov_b64_e32 v[152:153], v[56:57]
	v_mov_b64_e32 v[150:151], v[54:55]
	v_mov_b64_e32 v[148:149], v[52:53]
	v_mov_b64_e32 v[146:147], v[50:51]
	v_mov_b64_e32 v[144:145], v[48:49]
	v_mov_b64_e32 v[142:143], v[46:47]
	v_mov_b64_e32 v[138:139], v[58:59]
	v_mov_b64_e32 v[136:137], v[56:57]
	v_mov_b64_e32 v[134:135], v[54:55]
	v_mov_b64_e32 v[132:133], v[52:53]
	v_mov_b64_e32 v[130:131], v[50:51]
	v_mov_b64_e32 v[128:129], v[48:49]
	v_mov_b64_e32 v[126:127], v[46:47]
	v_mov_b64_e32 v[122:123], v[58:59]
	v_mov_b64_e32 v[120:121], v[56:57]
	v_mov_b64_e32 v[118:119], v[54:55]
	v_mov_b64_e32 v[116:117], v[52:53]
	v_mov_b64_e32 v[114:115], v[50:51]
	v_mov_b64_e32 v[112:113], v[48:49]
	v_mov_b64_e32 v[110:111], v[46:47]
	v_mov_b64_e32 v[106:107], v[58:59]
	v_mov_b64_e32 v[104:105], v[56:57]
	v_mov_b64_e32 v[102:103], v[54:55]
	v_mov_b64_e32 v[100:101], v[52:53]
	v_mov_b64_e32 v[98:99], v[50:51]
	v_mov_b64_e32 v[96:97], v[48:49]
	v_mov_b64_e32 v[94:95], v[46:47]

; #define LAS __attribute__((address_space(3)))
; __device__ __forceinline__ bf16x8 nsa_pack8(const f32x16& p, int s) { u32x4 w; w.x = pg8::cvt_pk_bf16(p[8 * s + 0], p[8 * s + 1]); w.y = pg8::cvt_pk_bf16(p[8 * s + 2], p[8 * s + 3]); w.z = pg8::cvt_pk_bf16(p[8 * s + 4], p[8 * s + 5]); w.w = pg8::cvt_pk_bf16(p[8 * s + 6], p[8 * s + 7]); return __builtin_bit_cast(bf16x8, w); }
; __device__ __forceinline__ void nsa_pv_rd4(const LAS unsigned char* vA, int sv, int step, bf16x8 (&af)[4]) {
; #pragma unroll
;     for (int dt = 0; dt < 4; ++dt) af[dt] = *(const LAS bf16x8*)(vA + dt * 4096 + (((2 * step) * 16) ^ sv));
; }
; __device__ __forceinline__ void nsa_pv_mm4(const bf16x8 (&af)[4], const bf16x8& pfk, f32x16 (&o)[4]) {
; #pragma unroll
;     for (int dt = 0; dt < 4; ++dt) o[dt] = __builtin_amdgcn_mfma_f32_32x32x16_bf16(af[dt], pfk, o[dt], 0, 0, 0);
; }
; __device__ __forceinline__ void nsa_pv_sw(const LAS unsigned char* vbuf, const bf16x8 (&pf)[2][2], f32x16 (&o)[4], int r, int h) {
;     const int sv = (((r >> 1) & 7) ^ h) * 16; const LAS unsigned char* vA = vbuf + r * 128;
; #pragma unroll
;     for (int step = 0; step < 4; ++step) { bf16x8 fa[4];
;         nsa_pv_rd4(vA, sv, step, fa); __builtin_amdgcn_sched_barrier(0);
;         nsa_pv_mm4(fa, pf[step >> 1][step & 1], o); __builtin_amdgcn_sched_barrier(0); }
; __device__ __forceinline__ void nsa_unit(const Args& a, LAS unsigned char* lds, int b, int kvh, int qb) {
;     ...
;             const float nmc = lane_on ? -mrun * SM_C : NINF;
;             float ls = 0.f;
; #pragma unroll
;             for (int i = 0; i < 16; ++i) { p0[i] = __builtin_amdgcn_exp2f(fmaf(p0[i], SM_C, nmc)); p1[i] = __builtin_amdgcn_exp2f(fmaf(p1[i], SM_C, nmc)); ls += p0[i] + p1[i]; }
;             lrun = lrun * alpha + ls;
;             pf[0][0] = nsa_pack8(p0, 0); pf[0][1] = nsa_pack8(p0, 1); pf[1][0] = nsa_pack8(p1, 0); pf[1][1] = nsa_pack8(p1, 1);
.LBB0_1857:
	v_mul_f32_e32 v34, 0xbe0293ee, v208
	v_cndmask_b32_e64 v190, v244, v34, s[2:3]
	v_fmamk_f32 v34, v78, 0x3e0293ee, v190
	v_exp_f32_e32 v78, v34
	v_fmamk_f32 v34, v62, 0x3e0293ee, v190
	v_exp_f32_e32 v62, v34
	v_fmamk_f32 v34, v79, 0x3e0293ee, v190
	v_fmamk_f32 v36, v80, 0x3e0293ee, v190
	v_exp_f32_e32 v79, v34
	v_fmamk_f32 v34, v63, 0x3e0293ee, v190
	v_exp_f32_e32 v80, v36
	v_fmamk_f32 v36, v64, 0x3e0293ee, v190
	v_exp_f32_e32 v63, v34
	v_exp_f32_e32 v64, v36
	v_fmamk_f32 v36, v81, 0x3e0293ee, v190
	v_exp_f32_e32 v81, v36
	v_fmamk_f32 v36, v65, 0x3e0293ee, v190
	v_exp_f32_e32 v65, v36
	v_add_f32_e32 v34, v78, v62
	v_add_f32_e32 v34, 0, v34
	v_add_f32_e32 v35, v79, v63
	v_add_f32_e32 v34, v35, v34
	v_add_f32_e32 v35, v80, v64
	v_add_f32_e32 v34, v35, v34
	v_add_f32_e32 v35, v81, v65
	v_add_f32_e32 v50, v35, v34
	v_fmamk_f32 v34, v82, 0x3e0293ee, v190
	v_exp_f32_e32 v35, v34
	v_fmamk_f32 v34, v66, 0x3e0293ee, v190
	v_exp_f32_e32 v37, v34
	v_fmamk_f32 v34, v83, 0x3e0293ee, v190
	v_fmamk_f32 v36, v67, 0x3e0293ee, v190
	v_fmamk_f32 v38, v84, 0x3e0293ee, v190
	v_exp_f32_e32 v34, v34
	v_exp_f32_e32 v36, v36
	v_exp_f32_e32 v39, v38
	v_fmamk_f32 v38, v68, 0x3e0293ee, v190
	v_exp_f32_e32 v41, v38
	v_fmamk_f32 v38, v85, 0x3e0293ee, v190
	v_fmamk_f32 v40, v69, 0x3e0293ee, v190
	v_exp_f32_e32 v38, v38
	v_exp_f32_e32 v40, v40
	v_pk_add_f32 v[48:49], v[34:35], v[36:37]
	v_fmamk_f32 v52, v88, 0x3e0293ee, v190
	v_add_f32_e32 v49, v49, v50
	v_add_f32_e32 v50, v48, v49
	v_pk_add_f32 v[48:49], v[38:39], v[40:41]
	v_exp_f32_e32 v53, v52
	v_add_f32_e32 v49, v49, v50
	v_add_f32_e32 v58, v48, v49
	v_fmamk_f32 v48, v86, 0x3e0293ee, v190
	v_exp_f32_e32 v49, v48
	v_fmamk_f32 v48, v70, 0x3e0293ee, v190
	v_exp_f32_e32 v51, v48
	v_fmamk_f32 v48, v87, 0x3e0293ee, v190
	v_fmamk_f32 v50, v71, 0x3e0293ee, v190
	v_exp_f32_e32 v48, v48
	v_exp_f32_e32 v50, v50
	v_fmamk_f32 v52, v72, 0x3e0293ee, v190
	v_exp_f32_e32 v55, v52
	v_fmamk_f32 v52, v89, 0x3e0293ee, v190
	v_fmamk_f32 v54, v73, 0x3e0293ee, v190
	v_exp_f32_e32 v52, v52
	v_exp_f32_e32 v54, v54
	v_pk_add_f32 v[56:57], v[48:49], v[50:51]
	v_fmamk_f32 v60, v92, 0x3e0293ee, v190
	v_add_f32_e32 v57, v57, v58
	v_add_f32_e32 v58, v56, v57
	v_pk_add_f32 v[56:57], v[52:53], v[54:55]
	v_exp_f32_e32 v61, v60
	v_add_f32_e32 v57, v57, v58
	v_add_f32_e32 v68, v56, v57
	v_fmamk_f32 v56, v90, 0x3e0293ee, v190
	v_exp_f32_e32 v57, v56
	v_fmamk_f32 v56, v74, 0x3e0293ee, v190
	v_exp_f32_e32 v59, v56
	v_fmamk_f32 v56, v91, 0x3e0293ee, v190
	v_fmamk_f32 v58, v75, 0x3e0293ee, v190
	v_exp_f32_e32 v56, v56
	v_exp_f32_e32 v58, v58
	v_fmamk_f32 v60, v76, 0x3e0293ee, v190
	v_exp_f32_e32 v211, v60
	v_fmamk_f32 v60, v93, 0x3e0293ee, v190
	v_fmac_f32_e32 v190, 0x3e0293ee, v77
	v_exp_f32_e32 v60, v60
	v_exp_f32_e32 v210, v190
	v_pk_add_f32 v[66:67], v[56:57], v[58:59]
	v_add_f32_e32 v67, v67, v68
	v_add_f32_e32 v66, v66, v67
	v_pk_add_f32 v[190:191], v[60:61], v[210:211]
	v_add_f32_e32 v191, v191, v66
	v_add_f32_e32 v212, v190, v191
	v_fmac_f32_e32 v212, v209, v46
	v_mov_b32_e32 v209, v212
	v_cvt_pk_bf16_f32 v190, v78, v79
	v_cvt_pk_bf16_f32 v191, v80, v81
	v_cvt_pk_bf16_f32 v192, v35, v34
	v_cvt_pk_bf16_f32 v193, v39, v38
	v_cvt_pk_bf16_f32 v194, v49, v48
	v_cvt_pk_bf16_f32 v195, v53, v52
	v_cvt_pk_bf16_f32 v196, v57, v56
	v_cvt_pk_bf16_f32 v197, v61, v60
	v_cvt_pk_bf16_f32 v198, v62, v63
	v_cvt_pk_bf16_f32 v199, v64, v65
	v_cvt_pk_bf16_f32 v200, v37, v36
	v_cvt_pk_bf16_f32 v201, v41, v40
	v_cvt_pk_bf16_f32 v202, v51, v50
	v_cvt_pk_bf16_f32 v203, v55, v54
	v_cvt_pk_bf16_f32 v204, v59, v58
	v_cvt_pk_bf16_f32 v205, v211, v210
	v_mov_b32_e32 v210, v222
	v_mov_b32_e32 v211, v45
	s_and_b32 s33, s71, 0xc000
	v_lshrrev_b32_e32 v34, 1, v210
	s_add_i32 s33, s33, 0
	v_bitop3_b32 v34, v34, v211, 7 bitop3:0x6c
	v_lshlrev_b32_e32 v46, 4, v34
	v_lshl_add_u32 v56, v210, 7, s33
	v_add_u32_e32 v212, v56, v46
	ds_read_b128 v[34:37], v212 offset:49152
	ds_read_b128 v[38:41], v212 offset:53248
	ds_read_b128 v[48:51], v212 offset:57344
	ds_read_b128 v[52:55], v212 offset:61440
	s_waitcnt lgkmcnt(3)
	v_mfma_f32_32x32x16_bf16 v[142:157], v[34:37], v[190:193], v[142:157]
	s_waitcnt lgkmcnt(2)
	v_mfma_f32_32x32x16_bf16 v[126:141], v[38:41], v[190:193], v[126:141]
	s_waitcnt lgkmcnt(1)
	v_mfma_f32_32x32x16_bf16 v[110:125], v[48:51], v[190:193], v[110:125]
	s_waitcnt lgkmcnt(0)
	v_mfma_f32_32x32x16_bf16 v[94:109], v[52:55], v[190:193], v[94:109]

; #define GAS __attribute__((address_space(1)))
; #define LAS __attribute__((address_space(3)))
; __device__ __forceinline__ unsigned cvt_pk_bf16(float lo, float hi) { unsigned r; asm volatile("v_cvt_pk_bf16_f32 %0, %1, %2" : "=v"(r) : "v"(lo), "v"(hi)); return r; }
; __device__ __forceinline__ void nsa_pv_rd4(const LAS unsigned char* vA, int sv, int step, bf16x8 (&af)[4]) {
; #pragma unroll
;     for (int dt = 0; dt < 4; ++dt) af[dt] = *(const LAS bf16x8*)(vA + dt * 4096 + (((2 * step) * 16) ^ sv));
; }
; __device__ __forceinline__ void nsa_pv_mm4(const bf16x8 (&af)[4], const bf16x8& pfk, f32x16 (&o)[4]) {
; #pragma unroll
;     for (int dt = 0; dt < 4; ++dt) o[dt] = __builtin_amdgcn_mfma_f32_32x32x16_bf16(af[dt], pfk, o[dt], 0, 0, 0);
; }
; __device__ __forceinline__ void nsa_pv_sw(const LAS unsigned char* vbuf, const bf16x8 (&pf)[2][2], f32x16 (&o)[4], int r, int h) {
;     const int sv = (((r >> 1) & 7) ^ h) * 16; const LAS unsigned char* vA = vbuf + r * 128;
; #pragma unroll
;     for (int step = 0; step < 4; ++step) { bf16x8 fa[4];
;         nsa_pv_rd4(vA, sv, step, fa); __builtin_amdgcn_sched_barrier(0);
;         nsa_pv_mm4(fa, pf[step >> 1][step & 1], o); __builtin_amdgcn_sched_barrier(0); }
; __device__ __forceinline__ void nsa_unit(const Args& a, LAS unsigned char* lds, int b, int kvh, int qb) {
;     ...
;         int ro = r, ho = h; asm volatile("" : "+v"(ro), "+v"(ho));
;         if (it > 0) { const int ti = it - 1;
;             nsa_pv_sw(lds + VOFF + (ti & 3) * NTB, pf, o, ro, ho);
;             if (ti == nS - 1 || ti == nTot - 1) {
;                 const float lt = lrun + __shfl_xor(lrun, 32); const float f = ((ti == nS - 1) ? g1 : g2) / lt;
; #pragma unroll
;                 for (int dt = 0; dt < 4; ++dt) {
; #pragma unroll
;                     for (int aa = 0; aa < 4; ++aa) { const u32x2 pv = *(const GAS u32x2*)(mp + (32 * dt + 8 * aa) * 2); u32x2 wv;
;                         wv.x = pg8::cvt_pk_bf16(bflo(pv.x) + o[dt][4 * aa] * f, bfhi(pv.x) + o[dt][4 * aa + 1] * f); wv.y = pg8::cvt_pk_bf16(bflo(pv.y) + o[dt][4 * aa + 2] * f, bfhi(pv.y) + o[dt][4 * aa + 3] * f);
;                         *(GAS u32x2*)(mp + (32 * dt + 8 * aa) * 2) = wv; }
.LBB0_1860:
	v_mov_b32_e32 v210, v222
	v_mov_b32_e32 v211, v45
	s_andn2_b64 vcc, exec, s[0:1]
	s_cbranch_vccnz .LBB0_1863
	s_and_b32 s0, s71, 0xc000
	v_lshrrev_b32_e32 v34, 1, v210
	s_add_i32 s0, s0, 0
	v_bitop3_b32 v34, v34, v211, 7 bitop3:0x6c
	v_lshlrev_b32_e32 v46, 4, v34
	v_lshl_add_u32 v56, v210, 7, s0
	v_xad_u32 v213, v46, 32, v56
	v_xad_u32 v214, v46, 64, v56
	v_xad_u32 v215, v46, s60, v56
	ds_read_b128 v[62:65], v213 offset:49152
	ds_read_b128 v[66:69], v213 offset:53248
	ds_read_b128 v[70:73], v213 offset:57344
	ds_read_b128 v[74:77], v213 offset:61440
	ds_read_b128 v[78:81], v214 offset:49152
	ds_read_b128 v[82:85], v214 offset:53248
	ds_read_b128 v[86:89], v214 offset:57344
	ds_read_b128 v[90:93], v214 offset:61440
	ds_read_b128 v[34:37], v215 offset:49152
	ds_read_b128 v[38:41], v215 offset:53248
	ds_read_b128 v[48:51], v215 offset:57344
	ds_read_b128 v[52:55], v215 offset:61440
	s_waitcnt lgkmcnt(11)
	v_mfma_f32_32x32x16_bf16 v[142:157], v[62:65], v[194:197], v[142:157]
	s_waitcnt lgkmcnt(10)
	v_mfma_f32_32x32x16_bf16 v[126:141], v[66:69], v[194:197], v[126:141]
	s_waitcnt lgkmcnt(9)
	v_mfma_f32_32x32x16_bf16 v[110:125], v[70:73], v[194:197], v[110:125]
	s_waitcnt lgkmcnt(8)
	v_mfma_f32_32x32x16_bf16 v[94:109], v[74:77], v[194:197], v[94:109]
	s_waitcnt lgkmcnt(7)
	v_mfma_f32_32x32x16_bf16 v[142:157], v[78:81], v[198:201], v[142:157]
	s_waitcnt lgkmcnt(6)
	v_mfma_f32_32x32x16_bf16 v[126:141], v[82:85], v[198:201], v[126:141]
	s_waitcnt lgkmcnt(5)
	v_mfma_f32_32x32x16_bf16 v[110:125], v[86:89], v[198:201], v[110:125]
	s_waitcnt lgkmcnt(4)
	v_mfma_f32_32x32x16_bf16 v[94:109], v[90:93], v[198:201], v[94:109]
	s_waitcnt lgkmcnt(3)
	v_mfma_f32_32x32x16_bf16 v[142:157], v[34:37], v[202:205], v[142:157]
	s_waitcnt lgkmcnt(2)
	v_mfma_f32_32x32x16_bf16 v[126:141], v[38:41], v[202:205], v[126:141]
	s_waitcnt lgkmcnt(1)
	v_mfma_f32_32x32x16_bf16 v[110:125], v[48:51], v[202:205], v[110:125]
	s_waitcnt lgkmcnt(0)
	v_mfma_f32_32x32x16_bf16 v[94:109], v[52:55], v[202:205], v[94:109]
	s_cmp_eq_u32 s16, s70
	s_cselect_b64 s[12:13], -1, 0
	s_cmp_eq_u32 s57, s70
	s_cselect_b64 s[0:1], -1, 0
	s_or_b64 s[0:1], s[12:13], s[0:1]
	s_andn2_b64 vcc, exec, s[0:1]
	s_cbranch_vccnz .LBB0_1863
	ds_bpermute_b32 v233, v252, v209
	v_cndmask_b32_e64 v208, v251, v250, s[12:13]
	v_mov_b32_e32 v60, v47
	v_mov_b32_e32 v61, v47
	v_mov_b32_e32 v48, v47
	s_waitcnt lgkmcnt(0)
	v_pk_add_f32 v[34:35], v[208:209], v[232:233]
	v_mov_b32_e32 v49, v47
	v_div_scale_f32 v36, s[0:1], v34, v34, 1.0
	v_rcp_f32_e32 v37, v36
	v_mov_b32_e32 v50, v47
	v_mov_b32_e32 v51, v47
	v_mov_b32_e32 v52, v47
	v_fma_f32 v38, -v36, v37, 1.0
	v_fmac_f32_e32 v37, v38, v37
	v_div_scale_f32 v38, vcc, 1.0, v34, 1.0
	v_mul_f32_e32 v39, v38, v37
	v_fma_f32 v40, -v36, v39, v38
	v_fmac_f32_e32 v39, v40, v37
	v_fma_f32 v36, -v36, v39, v38
	v_div_fmas_f32 v36, v36, v37, v39
	v_div_fixup_f32 v34, v36, v34, 1.0
	v_div_scale_f32 v36, s[0:1], v35, v35, v34
	v_rcp_f32_e32 v37, v36
	v_mov_b32_e32 v53, v47
	v_mov_b32_e32 v54, v47
	v_mov_b32_e32 v55, v47
	v_fma_f32 v38, -v36, v37, 1.0
	v_fmac_f32_e32 v37, v38, v37
	v_div_scale_f32 v38, vcc, v34, v35, v34
	v_mul_f32_e32 v39, v38, v37
	v_fma_f32 v40, -v36, v39, v38
	v_fmac_f32_e32 v39, v40, v37
	v_fma_f32 v36, -v36, v39, v38
	v_div_fmas_f32 v36, v36, v37, v39
	v_div_fixup_f32 v46, v36, v35, v34
	v_mov_b32_e32 v56, v47
	v_mov_b32_e32 v57, v47
	v_mov_b32_e32 v58, v47
	v_mov_b32_e32 v59, v47
	v_mov_b32_e32 v208, 0xf149f2ca
	v_mov_b32_e32 v209, 0
	global_load_dwordx2 v[62:63], v[206:207], off
	global_load_dwordx2 v[64:65], v[206:207], off offset:16
	global_load_dwordx2 v[66:67], v[206:207], off offset:32
	global_load_dwordx2 v[68:69], v[206:207], off offset:48
	global_load_dwordx2 v[70:71], v[206:207], off offset:64
	global_load_dwordx2 v[72:73], v[206:207], off offset:80
	global_load_dwordx2 v[74:75], v[206:207], off offset:96
	global_load_dwordx2 v[76:77], v[206:207], off offset:112
	global_load_dwordx2 v[78:79], v[206:207], off offset:128
	global_load_dwordx2 v[80:81], v[206:207], off offset:144
	global_load_dwordx2 v[82:83], v[206:207], off offset:160
	global_load_dwordx2 v[84:85], v[206:207], off offset:176
	global_load_dwordx2 v[86:87], v[206:207], off offset:192
	global_load_dwordx2 v[88:89], v[206:207], off offset:208
	global_load_dwordx2 v[90:91], v[206:207], off offset:224
	global_load_dwordx2 v[92:93], v[206:207], off offset:240
	s_waitcnt vmcnt(15)
	v_lshlrev_b32_e32 v36, 16, v62
	v_and_b32_e32 v34, 0xffff0000, v62
	v_fmac_f32_e32 v36, v142, v46
	v_fmac_f32_e32 v34, v143, v46
	v_cvt_pk_bf16_f32 v34, v36, v34
	v_lshlrev_b32_e32 v36, 16, v63
	v_and_b32_e32 v35, 0xffff0000, v63
	v_fmac_f32_e32 v35, v145, v46
	v_fmac_f32_e32 v36, v144, v46
	v_cvt_pk_bf16_f32 v35, v36, v35
	global_store_dwordx2 v[206:207], v[34:35], off
	s_waitcnt vmcnt(15)
	v_lshlrev_b32_e32 v36, 16, v64
	v_and_b32_e32 v34, 0xffff0000, v64
	v_fmac_f32_e32 v36, v146, v46
	v_fmac_f32_e32 v34, v147, v46
	v_cvt_pk_bf16_f32 v34, v36, v34
	v_lshlrev_b32_e32 v36, 16, v65
	v_and_b32_e32 v35, 0xffff0000, v65
	v_fmac_f32_e32 v35, v149, v46
	v_fmac_f32_e32 v36, v148, v46
	v_cvt_pk_bf16_f32 v35, v36, v35
	global_store_dwordx2 v[206:207], v[34:35], off offset:16
	s_waitcnt vmcnt(15)
	v_lshlrev_b32_e32 v36, 16, v66
	v_and_b32_e32 v34, 0xffff0000, v66
	v_fmac_f32_e32 v36, v150, v46
	v_fmac_f32_e32 v34, v151, v46
	v_cvt_pk_bf16_f32 v34, v36, v34
	v_lshlrev_b32_e32 v36, 16, v67
	v_and_b32_e32 v35, 0xffff0000, v67
	v_fmac_f32_e32 v35, v153, v46
	v_fmac_f32_e32 v36, v152, v46
	v_cvt_pk_bf16_f32 v35, v36, v35
	global_store_dwordx2 v[206:207], v[34:35], off offset:32
	s_waitcnt vmcnt(15)
; #define GAS __attribute__((address_space(1)))
; __device__ __forceinline__ unsigned cvt_pk_bf16(float lo, float hi) { unsigned r; asm volatile("v_cvt_pk_bf16_f32 %0, %1, %2" : "=v"(r) : "v"(lo), "v"(hi)); return r; }
; __device__ __forceinline__ void nsa_unit(const Args& a, LAS unsigned char* lds, int b, int kvh, int qb) {
;     ...
;                 const float lt = lrun + __shfl_xor(lrun, 32); const float f = ((ti == nS - 1) ? g1 : g2) / lt;
; #pragma unroll
;                 for (int dt = 0; dt < 4; ++dt) {
; #pragma unroll
;                     for (int aa = 0; aa < 4; ++aa) { const u32x2 pv = *(const GAS u32x2*)(mp + (32 * dt + 8 * aa) * 2); u32x2 wv;
;                         wv.x = pg8::cvt_pk_bf16(bflo(pv.x) + o[dt][4 * aa] * f, bfhi(pv.x) + o[dt][4 * aa + 1] * f); wv.y = pg8::cvt_pk_bf16(bflo(pv.y) + o[dt][4 * aa + 2] * f, bfhi(pv.y) + o[dt][4 * aa + 3] * f);
;                         *(GAS u32x2*)(mp + (32 * dt + 8 * aa) * 2) = wv; }
; #pragma unroll
;                     for (int i = 0; i < 16; ++i) o[dt][i] = 0.f; }
;                 mrun = -1e30f; lrun = 0.f;
;                 asm volatile("s_waitcnt vmcnt(0)" ::: "memory");
	v_lshlrev_b32_e32 v36, 16, v68
	v_and_b32_e32 v34, 0xffff0000, v68
	v_fmac_f32_e32 v36, v154, v46
	v_fmac_f32_e32 v34, v155, v46
	v_cvt_pk_bf16_f32 v34, v36, v34
	v_lshlrev_b32_e32 v36, 16, v69
	v_and_b32_e32 v35, 0xffff0000, v69
	v_fmac_f32_e32 v35, v157, v46
	v_fmac_f32_e32 v36, v156, v46
	v_cvt_pk_bf16_f32 v35, v36, v35
	global_store_dwordx2 v[206:207], v[34:35], off offset:48
	s_waitcnt vmcnt(15)
	v_lshlrev_b32_e32 v36, 16, v70
	v_and_b32_e32 v34, 0xffff0000, v70
	v_fmac_f32_e32 v36, v126, v46
	v_fmac_f32_e32 v34, v127, v46
	v_cvt_pk_bf16_f32 v34, v36, v34
	v_lshlrev_b32_e32 v36, 16, v71
	v_and_b32_e32 v35, 0xffff0000, v71
	v_fmac_f32_e32 v35, v129, v46
	v_fmac_f32_e32 v36, v128, v46
	v_cvt_pk_bf16_f32 v35, v36, v35
	global_store_dwordx2 v[206:207], v[34:35], off offset:64
	s_waitcnt vmcnt(15)
	v_lshlrev_b32_e32 v36, 16, v72
	v_and_b32_e32 v34, 0xffff0000, v72
	v_fmac_f32_e32 v36, v130, v46
	v_fmac_f32_e32 v34, v131, v46
	v_cvt_pk_bf16_f32 v34, v36, v34
	v_lshlrev_b32_e32 v36, 16, v73
	v_and_b32_e32 v35, 0xffff0000, v73
	v_fmac_f32_e32 v35, v133, v46
	v_fmac_f32_e32 v36, v132, v46
	v_cvt_pk_bf16_f32 v35, v36, v35
	global_store_dwordx2 v[206:207], v[34:35], off offset:80
	s_waitcnt vmcnt(15)
	v_lshlrev_b32_e32 v36, 16, v74
	v_and_b32_e32 v34, 0xffff0000, v74
	v_fmac_f32_e32 v36, v134, v46
	v_fmac_f32_e32 v34, v135, v46
	v_cvt_pk_bf16_f32 v34, v36, v34
	v_lshlrev_b32_e32 v36, 16, v75
	v_and_b32_e32 v35, 0xffff0000, v75
	v_fmac_f32_e32 v35, v137, v46
	v_fmac_f32_e32 v36, v136, v46
	v_cvt_pk_bf16_f32 v35, v36, v35
	global_store_dwordx2 v[206:207], v[34:35], off offset:96
	s_waitcnt vmcnt(15)
	v_lshlrev_b32_e32 v36, 16, v76
	v_and_b32_e32 v34, 0xffff0000, v76
	v_fmac_f32_e32 v36, v138, v46
	v_fmac_f32_e32 v34, v139, v46
	v_cvt_pk_bf16_f32 v34, v36, v34
	v_lshlrev_b32_e32 v36, 16, v77
	v_and_b32_e32 v35, 0xffff0000, v77
	v_fmac_f32_e32 v35, v141, v46
	v_fmac_f32_e32 v36, v140, v46
	v_cvt_pk_bf16_f32 v35, v36, v35
	global_store_dwordx2 v[206:207], v[34:35], off offset:112
	s_waitcnt vmcnt(15)
	v_lshlrev_b32_e32 v36, 16, v78
	v_and_b32_e32 v34, 0xffff0000, v78
	v_fmac_f32_e32 v36, v110, v46
	v_fmac_f32_e32 v34, v111, v46
	v_cvt_pk_bf16_f32 v34, v36, v34
	v_lshlrev_b32_e32 v36, 16, v79
	v_and_b32_e32 v35, 0xffff0000, v79
	v_fmac_f32_e32 v35, v113, v46
	v_fmac_f32_e32 v36, v112, v46
	v_cvt_pk_bf16_f32 v35, v36, v35
	global_store_dwordx2 v[206:207], v[34:35], off offset:128
	s_waitcnt vmcnt(15)
	v_lshlrev_b32_e32 v36, 16, v80
	v_and_b32_e32 v34, 0xffff0000, v80
	v_fmac_f32_e32 v36, v114, v46
	v_fmac_f32_e32 v34, v115, v46
	v_cvt_pk_bf16_f32 v34, v36, v34
	v_lshlrev_b32_e32 v36, 16, v81
	v_and_b32_e32 v35, 0xffff0000, v81
	v_fmac_f32_e32 v35, v117, v46
	v_fmac_f32_e32 v36, v116, v46
	v_cvt_pk_bf16_f32 v35, v36, v35
	global_store_dwordx2 v[206:207], v[34:35], off offset:144
	s_waitcnt vmcnt(15)
	v_lshlrev_b32_e32 v36, 16, v82
	v_and_b32_e32 v34, 0xffff0000, v82
	v_fmac_f32_e32 v36, v118, v46
	v_fmac_f32_e32 v34, v119, v46
	v_cvt_pk_bf16_f32 v34, v36, v34
	v_lshlrev_b32_e32 v36, 16, v83
	v_and_b32_e32 v35, 0xffff0000, v83
	v_fmac_f32_e32 v35, v121, v46
	v_fmac_f32_e32 v36, v120, v46
	v_cvt_pk_bf16_f32 v35, v36, v35
	global_store_dwordx2 v[206:207], v[34:35], off offset:160
	s_waitcnt vmcnt(15)
	v_lshlrev_b32_e32 v36, 16, v84
	v_and_b32_e32 v34, 0xffff0000, v84
	v_fmac_f32_e32 v36, v122, v46
	v_fmac_f32_e32 v34, v123, v46
	v_cvt_pk_bf16_f32 v34, v36, v34
	v_lshlrev_b32_e32 v36, 16, v85
	v_and_b32_e32 v35, 0xffff0000, v85
	v_fmac_f32_e32 v35, v125, v46
	v_fmac_f32_e32 v36, v124, v46
	v_cvt_pk_bf16_f32 v35, v36, v35
	global_store_dwordx2 v[206:207], v[34:35], off offset:176
	s_waitcnt vmcnt(15)
	v_lshlrev_b32_e32 v36, 16, v86
	v_and_b32_e32 v34, 0xffff0000, v86
	v_fmac_f32_e32 v36, v94, v46
	v_fmac_f32_e32 v34, v95, v46
	v_cvt_pk_bf16_f32 v34, v36, v34
	v_lshlrev_b32_e32 v36, 16, v87
	v_and_b32_e32 v35, 0xffff0000, v87
	v_fmac_f32_e32 v35, v97, v46
	v_fmac_f32_e32 v36, v96, v46
	v_cvt_pk_bf16_f32 v35, v36, v35
	global_store_dwordx2 v[206:207], v[34:35], off offset:192
	s_waitcnt vmcnt(15)
	v_lshlrev_b32_e32 v36, 16, v88
	v_and_b32_e32 v34, 0xffff0000, v88
	v_fmac_f32_e32 v36, v98, v46
	v_fmac_f32_e32 v34, v99, v46
	v_cvt_pk_bf16_f32 v34, v36, v34
	v_lshlrev_b32_e32 v36, 16, v89
	v_and_b32_e32 v35, 0xffff0000, v89
	v_fmac_f32_e32 v35, v101, v46
	v_fmac_f32_e32 v36, v100, v46
	v_cvt_pk_bf16_f32 v35, v36, v35
	global_store_dwordx2 v[206:207], v[34:35], off offset:208
	s_waitcnt vmcnt(15)
	v_lshlrev_b32_e32 v36, 16, v90
	v_and_b32_e32 v34, 0xffff0000, v90
	v_fmac_f32_e32 v36, v102, v46
	v_fmac_f32_e32 v34, v103, v46
	v_cvt_pk_bf16_f32 v34, v36, v34
	v_lshlrev_b32_e32 v36, 16, v91
	v_and_b32_e32 v35, 0xffff0000, v91
	v_fmac_f32_e32 v35, v105, v46
	v_fmac_f32_e32 v36, v104, v46
	v_cvt_pk_bf16_f32 v35, v36, v35
	global_store_dwordx2 v[206:207], v[34:35], off offset:224
	s_waitcnt vmcnt(15)
	v_lshlrev_b32_e32 v36, 16, v92
	v_and_b32_e32 v34, 0xffff0000, v92
	v_fmac_f32_e32 v36, v106, v46
	v_fmac_f32_e32 v34, v107, v46
	v_cvt_pk_bf16_f32 v34, v36, v34
	v_lshlrev_b32_e32 v36, 16, v93
	v_and_b32_e32 v35, 0xffff0000, v93
	v_fmac_f32_e32 v35, v109, v46
	v_fmac_f32_e32 v36, v108, v46
	v_cvt_pk_bf16_f32 v35, v36, v35
	global_store_dwordx2 v[206:207], v[34:35], off offset:240
	s_waitcnt vmcnt(0)
	v_mov_b32_e32 v46, v47
	v_mov_b64_e32 v[156:157], v[60:61]
	v_mov_b64_e32 v[140:141], v[60:61]
	v_mov_b64_e32 v[124:125], v[60:61]
	v_mov_b64_e32 v[108:109], v[60:61]
	v_mov_b64_e32 v[154:155], v[58:59]
	v_mov_b64_e32 v[152:153], v[56:57]
	v_mov_b64_e32 v[150:151], v[54:55]
	v_mov_b64_e32 v[148:149], v[52:53]
	v_mov_b64_e32 v[146:147], v[50:51]
	v_mov_b64_e32 v[144:145], v[48:49]
	v_mov_b64_e32 v[142:143], v[46:47]
	v_mov_b64_e32 v[138:139], v[58:59]
	v_mov_b64_e32 v[136:137], v[56:57]
	v_mov_b64_e32 v[134:135], v[54:55]
	v_mov_b64_e32 v[132:133], v[52:53]
	v_mov_b64_e32 v[130:131], v[50:51]
	v_mov_b64_e32 v[128:129], v[48:49]
	v_mov_b64_e32 v[126:127], v[46:47]
	v_mov_b64_e32 v[122:123], v[58:59]
	v_mov_b64_e32 v[120:121], v[56:57]
	v_mov_b64_e32 v[118:119], v[54:55]
	v_mov_b64_e32 v[116:117], v[52:53]
	v_mov_b64_e32 v[114:115], v[50:51]
	v_mov_b64_e32 v[112:113], v[48:49]
	v_mov_b64_e32 v[110:111], v[46:47]
	v_mov_b64_e32 v[106:107], v[58:59]
	v_mov_b64_e32 v[104:105], v[56:57]
	v_mov_b64_e32 v[102:103], v[54:55]
	v_mov_b64_e32 v[100:101], v[52:53]
	v_mov_b64_e32 v[98:99], v[50:51]
	v_mov_b64_e32 v[96:97], v[48:49]
	v_mov_b64_e32 v[94:95], v[46:47]
